# baseline (speedup 1.0000x reference)
.Lpc_anchor:
	s_add_u32 s44, s44, _Z7dog_finPKfS0_Pf-.Lpc_anchor
	s_addc_u32 s45, s45, 0
	s_load_dwordx16 s[48:63], s[44:45], 0x0
	s_load_dwordx16 s[64:79], s[44:45], 0x40
	s_load_dwordx16 s[80:95], s[44:45], 0x80
	v_mul_f32_e32 v16, v12, v12
	v_add_f32_e32 v17, 0x3f800000, v12
	v_add_f32_e32 v18, 0x40000000, v12
	v_add_f32_e32 v19, 0x40400000, v12
	v_mul_f32_e32 v17, v17, v17
	v_mul_f32_e32 v18, v18, v18
	v_mul_f32_e32 v19, v19, v19
	v_mul_f32_e32 v20, v8, v16
	v_mul_f32_e32 v24, v9, v16
	v_mul_f32_e32 v21, v8, v17
	v_mul_f32_e32 v25, v9, v17
	v_mul_f32_e32 v22, v8, v18
	v_mul_f32_e32 v26, v9, v18
	v_mul_f32_e32 v23, v8, v19
	v_mul_f32_e32 v27, v9, v19
	v_exp_f32_e32 v20, v20
	v_exp_f32_e32 v21, v21
	v_exp_f32_e32 v22, v22
	v_exp_f32_e32 v23, v23
	v_exp_f32_e32 v24, v24
	v_exp_f32_e32 v25, v25
	v_exp_f32_e32 v26, v26
	v_exp_f32_e32 v27, v27
	v_cvt_pk_f16_f32 v32, v20, v21
	v_cvt_pk_f16_f32 v33, v22, v23
	v_cvt_pk_f16_f32 v64, v24, v25
	v_cvt_pk_f16_f32 v65, v26, v27
	v_add_f32_e32 v16, 0x40800000, v12
	v_add_f32_e32 v17, 0x40a00000, v12
	v_add_f32_e32 v18, 0x40c00000, v12
	v_add_f32_e32 v19, 0x40e00000, v12
	v_mul_f32_e32 v16, v16, v16
	v_mul_f32_e32 v17, v17, v17
	v_mul_f32_e32 v18, v18, v18
	v_mul_f32_e32 v19, v19, v19
	v_mul_f32_e32 v20, v8, v16
	v_mul_f32_e32 v24, v9, v16
	v_mul_f32_e32 v21, v8, v17
	v_mul_f32_e32 v25, v9, v17
	v_mul_f32_e32 v22, v8, v18
	v_mul_f32_e32 v26, v9, v18
	v_mul_f32_e32 v23, v8, v19
	v_mul_f32_e32 v27, v9, v19
	v_exp_f32_e32 v20, v20
	v_exp_f32_e32 v21, v21
	v_exp_f32_e32 v22, v22
	v_exp_f32_e32 v23, v23
	v_exp_f32_e32 v24, v24
	v_exp_f32_e32 v25, v25
	v_exp_f32_e32 v26, v26
	v_exp_f32_e32 v27, v27
	v_cvt_pk_f16_f32 v34, v20, v21
	v_cvt_pk_f16_f32 v35, v22, v23
	v_cvt_pk_f16_f32 v66, v24, v25
	v_cvt_pk_f16_f32 v67, v26, v27
	v_add_f32_e32 v16, 0x42000000, v12
	v_add_f32_e32 v17, 0x42040000, v12
	v_add_f32_e32 v18, 0x42080000, v12
	v_add_f32_e32 v19, 0x420c0000, v12
	v_mul_f32_e32 v16, v16, v16
	v_mul_f32_e32 v17, v17, v17
	v_mul_f32_e32 v18, v18, v18
	v_mul_f32_e32 v19, v19, v19
	v_mul_f32_e32 v20, v8, v16
	v_mul_f32_e32 v24, v9, v16
	v_mul_f32_e32 v21, v8, v17
	v_mul_f32_e32 v25, v9, v17
	v_mul_f32_e32 v22, v8, v18
	v_mul_f32_e32 v26, v9, v18
	v_mul_f32_e32 v23, v8, v19
	v_mul_f32_e32 v27, v9, v19
	v_exp_f32_e32 v20, v20
	v_exp_f32_e32 v21, v21
	v_exp_f32_e32 v22, v22
	v_exp_f32_e32 v23, v23
	v_exp_f32_e32 v24, v24
	v_exp_f32_e32 v25, v25
	v_exp_f32_e32 v26, v26
	v_exp_f32_e32 v27, v27
	v_cvt_pk_f16_f32 v36, v20, v21
	v_cvt_pk_f16_f32 v37, v22, v23
	v_cvt_pk_f16_f32 v68, v24, v25
	v_cvt_pk_f16_f32 v69, v26, v27
	v_add_f32_e32 v16, 0x42100000, v12
	v_add_f32_e32 v17, 0x42140000, v12
	v_add_f32_e32 v18, 0x42180000, v12
	v_add_f32_e32 v19, 0x421c0000, v12
	v_mul_f32_e32 v16, v16, v16
	v_mul_f32_e32 v17, v17, v17
	v_mul_f32_e32 v18, v18, v18
	v_mul_f32_e32 v19, v19, v19
	v_mul_f32_e32 v20, v8, v16
	v_mul_f32_e32 v24, v9, v16
	v_mul_f32_e32 v21, v8, v17
	v_mul_f32_e32 v25, v9, v17
	v_mul_f32_e32 v22, v8, v18
	v_mul_f32_e32 v26, v9, v18
	v_mul_f32_e32 v23, v8, v19
	v_mul_f32_e32 v27, v9, v19
	v_exp_f32_e32 v20, v20
	v_exp_f32_e32 v21, v21
	v_exp_f32_e32 v22, v22
	v_exp_f32_e32 v23, v23
	v_exp_f32_e32 v24, v24
	v_exp_f32_e32 v25, v25
	v_exp_f32_e32 v26, v26
	v_exp_f32_e32 v27, v27
	v_cvt_pk_f16_f32 v38, v20, v21
	v_cvt_pk_f16_f32 v39, v22, v23
	v_cvt_pk_f16_f32 v70, v24, v25
	v_cvt_pk_f16_f32 v71, v26, v27
	s_and_b32 s46, s0, 0xfff
	s_sub_u32 s46, s46, 0x80
	s_cmp_lt_u32 s46, 0xd00
	s_cbranch_scc0 .Lno_karg_touch
	s_load_dwordx16 s[48:63], s[0:1], -0x80
	s_load_dwordx16 s[64:79], s[0:1], -0x40
	s_load_dwordx16 s[80:95], s[0:1], 0x40
	s_load_dwordx16 s[48:63], s[0:1], 0x80
	s_load_dwordx16 s[64:79], s[0:1], 0xc0
	s_load_dwordx16 s[80:95], s[0:1], 0x100
	s_load_dwordx16 s[48:63], s[0:1], 0x140
.Lno_karg_touch:
	v_add_u32_e32 v6, 0x8000, v6
	global_load_dwordx4 v[160:163], v6, s[12:13] offset:0 nt
	global_load_dwordx4 v[164:167], v6, s[12:13] offset:1024 nt
	global_load_dwordx4 v[168:171], v6, s[12:13] offset:2048 nt
	global_load_dwordx4 v[172:175], v6, s[12:13] offset:3072 nt
	v_add_f32_e32 v16, 0x42800000, v12
	v_add_f32_e32 v17, 0x42820000, v12
	v_add_f32_e32 v18, 0x42840000, v12
	v_add_f32_e32 v19, 0x42860000, v12
	v_mul_f32_e32 v16, v16, v16
	v_mul_f32_e32 v17, v17, v17
	v_mul_f32_e32 v18, v18, v18
	v_mul_f32_e32 v19, v19, v19
	v_mul_f32_e32 v20, v8, v16
	v_mul_f32_e32 v24, v9, v16
	v_mul_f32_e32 v21, v8, v17
	v_mul_f32_e32 v25, v9, v17
	v_mul_f32_e32 v22, v8, v18
	v_mul_f32_e32 v26, v9, v18
	v_mul_f32_e32 v23, v8, v19
	v_mul_f32_e32 v27, v9, v19
	v_exp_f32_e32 v20, v20
	v_exp_f32_e32 v21, v21
	v_exp_f32_e32 v22, v22
	v_exp_f32_e32 v23, v23
	v_exp_f32_e32 v24, v24
	v_exp_f32_e32 v25, v25
	v_exp_f32_e32 v26, v26
	v_exp_f32_e32 v27, v27
	v_cvt_pk_f16_f32 v40, v20, v21
	v_cvt_pk_f16_f32 v41, v22, v23
	v_cvt_pk_f16_f32 v72, v24, v25
	v_cvt_pk_f16_f32 v73, v26, v27
	v_add_f32_e32 v16, 0x42880000, v12
	v_add_f32_e32 v17, 0x428a0000, v12
	v_add_f32_e32 v18, 0x428c0000, v12
	v_add_f32_e32 v19, 0x428e0000, v12
	v_mul_f32_e32 v16, v16, v16
	v_mul_f32_e32 v17, v17, v17
	v_mul_f32_e32 v18, v18, v18
	v_mul_f32_e32 v19, v19, v19
	v_mul_f32_e32 v20, v8, v16
	v_mul_f32_e32 v24, v9, v16
	v_mul_f32_e32 v21, v8, v17
	v_mul_f32_e32 v25, v9, v17
	v_mul_f32_e32 v22, v8, v18
	v_mul_f32_e32 v26, v9, v18
	v_mul_f32_e32 v23, v8, v19
	v_mul_f32_e32 v27, v9, v19
	v_exp_f32_e32 v20, v20
	v_exp_f32_e32 v21, v21
	v_exp_f32_e32 v22, v22
	v_exp_f32_e32 v23, v23
	v_exp_f32_e32 v24, v24
	v_exp_f32_e32 v25, v25
	v_exp_f32_e32 v26, v26
	v_exp_f32_e32 v27, v27
	v_cvt_pk_f16_f32 v42, v20, v21
	v_cvt_pk_f16_f32 v43, v22, v23
	v_cvt_pk_f16_f32 v74, v24, v25
	v_cvt_pk_f16_f32 v75, v26, v27
	v_add_f32_e32 v16, 0x42c00000, v12
	v_add_f32_e32 v17, 0x42c20000, v12
	v_add_f32_e32 v18, 0x42c40000, v12
	v_add_f32_e32 v19, 0x42c60000, v12
	v_mul_f32_e32 v16, v16, v16
	v_mul_f32_e32 v17, v17, v17
	v_mul_f32_e32 v18, v18, v18
	v_mul_f32_e32 v19, v19, v19
	v_mul_f32_e32 v20, v8, v16
	v_mul_f32_e32 v24, v9, v16
	v_mul_f32_e32 v21, v8, v17
	v_mul_f32_e32 v25, v9, v17
	v_mul_f32_e32 v22, v8, v18
	v_mul_f32_e32 v26, v9, v18
	v_mul_f32_e32 v23, v8, v19
	v_mul_f32_e32 v27, v9, v19
	v_exp_f32_e32 v20, v20
	v_exp_f32_e32 v21, v21
	v_exp_f32_e32 v22, v22
	v_exp_f32_e32 v23, v23
	v_exp_f32_e32 v24, v24
	v_exp_f32_e32 v25, v25
	v_exp_f32_e32 v26, v26
	v_exp_f32_e32 v27, v27
	v_cvt_pk_f16_f32 v44, v20, v21
	v_cvt_pk_f16_f32 v45, v22, v23
	v_cvt_pk_f16_f32 v76, v24, v25
	v_cvt_pk_f16_f32 v77, v26, v27
	v_add_f32_e32 v16, 0x42c80000, v12
	v_add_f32_e32 v17, 0x42ca0000, v12
	v_add_f32_e32 v18, 0x42cc0000, v12
	v_add_f32_e32 v19, 0x42ce0000, v12
	v_mul_f32_e32 v16, v16, v16
	v_mul_f32_e32 v17, v17, v17
	v_mul_f32_e32 v18, v18, v18
	v_mul_f32_e32 v19, v19, v19
	v_mul_f32_e32 v20, v8, v16
	v_mul_f32_e32 v24, v9, v16
	v_mul_f32_e32 v21, v8, v17
	v_mul_f32_e32 v25, v9, v17
	v_mul_f32_e32 v22, v8, v18
	v_mul_f32_e32 v26, v9, v18
	v_mul_f32_e32 v23, v8, v19
	v_mul_f32_e32 v27, v9, v19
	v_exp_f32_e32 v20, v20
	v_exp_f32_e32 v21, v21
	v_exp_f32_e32 v22, v22
	v_exp_f32_e32 v23, v23
	v_exp_f32_e32 v24, v24
	v_exp_f32_e32 v25, v25
	v_exp_f32_e32 v26, v26
	v_exp_f32_e32 v27, v27
	v_cvt_pk_f16_f32 v46, v20, v21
	v_cvt_pk_f16_f32 v47, v22, v23
	v_cvt_pk_f16_f32 v78, v24, v25
	v_cvt_pk_f16_f32 v79, v26, v27
	v_add_u32_e32 v6, 0x8000, v6
	global_load_dwordx4 v[176:179], v6, s[12:13] offset:0 nt
	global_load_dwordx4 v[180:183], v6, s[12:13] offset:1024 nt
	global_load_dwordx4 v[184:187], v6, s[12:13] offset:2048 nt
	global_load_dwordx4 v[188:191], v6, s[12:13] offset:3072 nt
	v_mul_f32_e32 v16, v2, v2
	v_add_f32_e32 v17, 0x3f800000, v2
	v_add_f32_e32 v18, 0x40000000, v2
	v_add_f32_e32 v19, 0x40400000, v2
	v_mul_f32_e32 v17, v17, v17
	v_mul_f32_e32 v18, v18, v18
	v_mul_f32_e32 v19, v19, v19
	v_mul_f32_e32 v20, v28, v16
	v_mul_f32_e32 v24, v29, v16
	v_mul_f32_e32 v21, v28, v17
	v_mul_f32_e32 v25, v29, v17
	v_mul_f32_e32 v22, v28, v18
	v_mul_f32_e32 v26, v29, v18
	v_mul_f32_e32 v23, v28, v19
	v_mul_f32_e32 v27, v29, v19
	v_exp_f32_e32 v20, v20
	v_exp_f32_e32 v21, v21
	v_exp_f32_e32 v22, v22
	v_exp_f32_e32 v23, v23
	v_exp_f32_e32 v24, v24
	v_exp_f32_e32 v25, v25
	v_exp_f32_e32 v26, v26
	v_exp_f32_e32 v27, v27
	v_cvt_pk_f16_f32 v48, v20, v21
	v_cvt_pk_f16_f32 v49, v22, v23
	v_cvt_pk_f16_f32 v80, v24, v25
	v_cvt_pk_f16_f32 v81, v26, v27
	v_add_f32_e32 v16, 0x40800000, v2
	v_add_f32_e32 v17, 0x40a00000, v2
	v_add_f32_e32 v18, 0x40c00000, v2
	v_add_f32_e32 v19, 0x40e00000, v2
	v_mul_f32_e32 v16, v16, v16
	v_mul_f32_e32 v17, v17, v17
	v_mul_f32_e32 v18, v18, v18
	v_mul_f32_e32 v19, v19, v19
	v_mul_f32_e32 v20, v28, v16
	v_mul_f32_e32 v24, v29, v16
	v_mul_f32_e32 v21, v28, v17
	v_mul_f32_e32 v25, v29, v17
	v_mul_f32_e32 v22, v28, v18
	v_mul_f32_e32 v26, v29, v18
	v_mul_f32_e32 v23, v28, v19
	v_mul_f32_e32 v27, v29, v19
	v_exp_f32_e32 v20, v20
	v_exp_f32_e32 v21, v21
	v_exp_f32_e32 v22, v22
	v_exp_f32_e32 v23, v23
	v_exp_f32_e32 v24, v24
	v_exp_f32_e32 v25, v25
	v_exp_f32_e32 v26, v26
	v_exp_f32_e32 v27, v27
	v_cvt_pk_f16_f32 v50, v20, v21
	v_cvt_pk_f16_f32 v51, v22, v23
	v_cvt_pk_f16_f32 v82, v24, v25
	v_cvt_pk_f16_f32 v83, v26, v27
	v_add_f32_e32 v16, 0x42000000, v2
	v_add_f32_e32 v17, 0x42040000, v2
	v_add_f32_e32 v18, 0x42080000, v2
	v_add_f32_e32 v19, 0x420c0000, v2
	v_mul_f32_e32 v16, v16, v16
	v_mul_f32_e32 v17, v17, v17
	v_mul_f32_e32 v18, v18, v18
	v_mul_f32_e32 v19, v19, v19
	v_mul_f32_e32 v20, v28, v16
	v_mul_f32_e32 v24, v29, v16
	v_mul_f32_e32 v21, v28, v17
	v_mul_f32_e32 v25, v29, v17
	v_mul_f32_e32 v22, v28, v18
	v_mul_f32_e32 v26, v29, v18
	v_mul_f32_e32 v23, v28, v19
	v_mul_f32_e32 v27, v29, v19
	v_exp_f32_e32 v20, v20
	v_exp_f32_e32 v21, v21
	v_exp_f32_e32 v22, v22
	v_exp_f32_e32 v23, v23
	v_exp_f32_e32 v24, v24
	v_exp_f32_e32 v25, v25
	v_exp_f32_e32 v26, v26
	v_exp_f32_e32 v27, v27
	v_cvt_pk_f16_f32 v52, v20, v21
	v_cvt_pk_f16_f32 v53, v22, v23
	v_cvt_pk_f16_f32 v84, v24, v25
	v_cvt_pk_f16_f32 v85, v26, v27
	v_add_f32_e32 v16, 0x42100000, v2
	v_add_f32_e32 v17, 0x42140000, v2
	v_add_f32_e32 v18, 0x42180000, v2
	v_add_f32_e32 v19, 0x421c0000, v2
	v_mul_f32_e32 v16, v16, v16
	v_mul_f32_e32 v17, v17, v17
	v_mul_f32_e32 v18, v18, v18
	v_mul_f32_e32 v19, v19, v19
	v_mul_f32_e32 v20, v28, v16
	v_mul_f32_e32 v24, v29, v16
	v_mul_f32_e32 v21, v28, v17
	v_mul_f32_e32 v25, v29, v17
	v_mul_f32_e32 v22, v28, v18
	v_mul_f32_e32 v26, v29, v18
	v_mul_f32_e32 v23, v28, v19
	v_mul_f32_e32 v27, v29, v19
	v_exp_f32_e32 v20, v20
	v_exp_f32_e32 v21, v21
	v_exp_f32_e32 v22, v22
	v_exp_f32_e32 v23, v23
	v_exp_f32_e32 v24, v24
	v_exp_f32_e32 v25, v25
	v_exp_f32_e32 v26, v26
	v_exp_f32_e32 v27, v27
	v_cvt_pk_f16_f32 v54, v20, v21
	v_cvt_pk_f16_f32 v55, v22, v23
	v_cvt_pk_f16_f32 v86, v24, v25
	v_cvt_pk_f16_f32 v87, v26, v27
	v_add_u32_e32 v6, 0x8000, v6
	global_load_dwordx4 v[192:195], v6, s[12:13] offset:0 nt
	global_load_dwordx4 v[196:199], v6, s[12:13] offset:1024 nt
	global_load_dwordx4 v[200:203], v6, s[12:13] offset:2048 nt
	global_load_dwordx4 v[204:207], v6, s[12:13] offset:3072 nt
	v_add_f32_e32 v16, 0x42800000, v2
	v_add_f32_e32 v17, 0x42820000, v2
	v_add_f32_e32 v18, 0x42840000, v2
	v_add_f32_e32 v19, 0x42860000, v2
	v_mul_f32_e32 v16, v16, v16
	v_mul_f32_e32 v17, v17, v17
	v_mul_f32_e32 v18, v18, v18
	v_mul_f32_e32 v19, v19, v19
	v_mul_f32_e32 v20, v28, v16
	v_mul_f32_e32 v24, v29, v16
	v_mul_f32_e32 v21, v28, v17
	v_mul_f32_e32 v25, v29, v17
	v_mul_f32_e32 v22, v28, v18
	v_mul_f32_e32 v26, v29, v18
	v_mul_f32_e32 v23, v28, v19
	v_mul_f32_e32 v27, v29, v19
	v_exp_f32_e32 v20, v20
	v_exp_f32_e32 v21, v21
	v_exp_f32_e32 v22, v22
	v_exp_f32_e32 v23, v23
	v_exp_f32_e32 v24, v24
	v_exp_f32_e32 v25, v25
	v_exp_f32_e32 v26, v26
	v_exp_f32_e32 v27, v27
	v_cvt_pk_f16_f32 v56, v20, v21
	v_cvt_pk_f16_f32 v57, v22, v23
	v_cvt_pk_f16_f32 v88, v24, v25
	v_cvt_pk_f16_f32 v89, v26, v27
	v_add_f32_e32 v16, 0x42880000, v2
	v_add_f32_e32 v17, 0x428a0000, v2
	v_add_f32_e32 v18, 0x428c0000, v2
	v_add_f32_e32 v19, 0x428e0000, v2
	v_mul_f32_e32 v16, v16, v16
	v_mul_f32_e32 v17, v17, v17
	v_mul_f32_e32 v18, v18, v18
	v_mul_f32_e32 v19, v19, v19
	v_mul_f32_e32 v20, v28, v16
	v_mul_f32_e32 v24, v29, v16
	v_mul_f32_e32 v21, v28, v17
	v_mul_f32_e32 v25, v29, v17
	v_mul_f32_e32 v22, v28, v18
	v_mul_f32_e32 v26, v29, v18
	v_mul_f32_e32 v23, v28, v19
	v_mul_f32_e32 v27, v29, v19
	v_exp_f32_e32 v20, v20
	v_exp_f32_e32 v21, v21
	v_exp_f32_e32 v22, v22
	v_exp_f32_e32 v23, v23
	v_exp_f32_e32 v24, v24
	v_exp_f32_e32 v25, v25
	v_exp_f32_e32 v26, v26
	v_exp_f32_e32 v27, v27
	v_cvt_pk_f16_f32 v58, v20, v21
	v_cvt_pk_f16_f32 v59, v22, v23
	v_cvt_pk_f16_f32 v90, v24, v25
	v_cvt_pk_f16_f32 v91, v26, v27
	v_add_f32_e32 v16, 0x42c00000, v2
	v_add_f32_e32 v17, 0x42c20000, v2
	v_add_f32_e32 v18, 0x42c40000, v2
	v_add_f32_e32 v19, 0x42c60000, v2
	v_mul_f32_e32 v16, v16, v16
	v_mul_f32_e32 v17, v17, v17
	v_mul_f32_e32 v18, v18, v18
	v_mul_f32_e32 v19, v19, v19
	v_mul_f32_e32 v20, v28, v16
	v_mul_f32_e32 v24, v29, v16
	v_mul_f32_e32 v21, v28, v17
	v_mul_f32_e32 v25, v29, v17
	v_mul_f32_e32 v22, v28, v18
	v_mul_f32_e32 v26, v29, v18
	v_mul_f32_e32 v23, v28, v19
	v_mul_f32_e32 v27, v29, v19
	v_exp_f32_e32 v20, v20
	v_exp_f32_e32 v21, v21
	v_exp_f32_e32 v22, v22
	v_exp_f32_e32 v23, v23
	v_exp_f32_e32 v24, v24
	v_exp_f32_e32 v25, v25
	v_exp_f32_e32 v26, v26
	v_exp_f32_e32 v27, v27
	v_cvt_pk_f16_f32 v60, v20, v21
	v_cvt_pk_f16_f32 v61, v22, v23
	v_cvt_pk_f16_f32 v92, v24, v25
	v_cvt_pk_f16_f32 v93, v26, v27
	v_add_f32_e32 v16, 0x42c80000, v2
	v_add_f32_e32 v17, 0x42ca0000, v2
	v_add_f32_e32 v18, 0x42cc0000, v2
	v_add_f32_e32 v19, 0x42ce0000, v2
	v_mul_f32_e32 v16, v16, v16
	v_mul_f32_e32 v17, v17, v17
	v_mul_f32_e32 v18, v18, v18
	v_mul_f32_e32 v19, v19, v19
	v_mul_f32_e32 v20, v28, v16
	v_mul_f32_e32 v24, v29, v16
	v_mul_f32_e32 v21, v28, v17
	v_mul_f32_e32 v25, v29, v17
	v_mul_f32_e32 v22, v28, v18
	v_mul_f32_e32 v26, v29, v18
	v_mul_f32_e32 v23, v28, v19
	v_mul_f32_e32 v27, v29, v19
	v_exp_f32_e32 v20, v20
	v_exp_f32_e32 v21, v21
	v_exp_f32_e32 v22, v22
	v_exp_f32_e32 v23, v23
	v_exp_f32_e32 v24, v24
	v_exp_f32_e32 v25, v25
	v_exp_f32_e32 v26, v26
	v_exp_f32_e32 v27, v27
	v_cvt_pk_f16_f32 v62, v20, v21
	v_cvt_pk_f16_f32 v63, v22, v23
	v_cvt_pk_f16_f32 v94, v24, v25
	v_cvt_pk_f16_f32 v95, v26, v27
	v_add_u32_e32 v6, 0x8000, v6
	global_load_dwordx4 v[208:211], v6, s[12:13] offset:0 nt
	global_load_dwordx4 v[212:215], v6, s[12:13] offset:1024 nt
	global_load_dwordx4 v[216:219], v6, s[12:13] offset:2048 nt
	global_load_dwordx4 v[220:223], v6, s[12:13] offset:3072 nt
	v_mul_f32_e32 v16, v13, v13
	v_add_f32_e32 v17, 0x3f800000, v13
	v_add_f32_e32 v18, 0x40000000, v13
	v_add_f32_e32 v19, 0x40400000, v13
	v_mul_f32_e32 v17, v17, v17
	v_mul_f32_e32 v18, v18, v18
	v_mul_f32_e32 v19, v19, v19
	v_mul_f32_e32 v20, v8, v16
	v_mul_f32_e32 v24, v9, v16
	v_mul_f32_e32 v21, v8, v17
	v_mul_f32_e32 v25, v9, v17
	v_mul_f32_e32 v22, v8, v18
	v_mul_f32_e32 v26, v9, v18
	v_mul_f32_e32 v23, v8, v19
	v_mul_f32_e32 v27, v9, v19
	v_exp_f32_e32 v20, v20
	v_exp_f32_e32 v21, v21
	v_exp_f32_e32 v22, v22
	v_exp_f32_e32 v23, v23
	v_exp_f32_e32 v24, v24
	v_exp_f32_e32 v25, v25
	v_exp_f32_e32 v26, v26
	v_exp_f32_e32 v27, v27
	v_mul_f32_e32 v96, v10, v20
	v_mul_f32_e32 v97, v10, v21
	v_mul_f32_e32 v98, v10, v22
	v_mul_f32_e32 v99, v10, v23
	v_mul_f32_e32 v112, v11, v24
	v_mul_f32_e32 v113, v11, v25
	v_mul_f32_e32 v114, v11, v26
	v_mul_f32_e32 v115, v11, v27
	v_add_f32_e32 v16, 0x41800000, v13
	v_add_f32_e32 v17, 0x41880000, v13
	v_add_f32_e32 v18, 0x41900000, v13
	v_add_f32_e32 v19, 0x41980000, v13
	v_mul_f32_e32 v16, v16, v16
	v_mul_f32_e32 v17, v17, v17
	v_mul_f32_e32 v18, v18, v18
	v_mul_f32_e32 v19, v19, v19
	v_mul_f32_e32 v20, v8, v16
	v_mul_f32_e32 v24, v9, v16
	v_mul_f32_e32 v21, v8, v17
	v_mul_f32_e32 v25, v9, v17
	v_mul_f32_e32 v22, v8, v18
	v_mul_f32_e32 v26, v9, v18
	v_mul_f32_e32 v23, v8, v19
	v_mul_f32_e32 v27, v9, v19
	v_exp_f32_e32 v20, v20
	v_exp_f32_e32 v21, v21
	v_exp_f32_e32 v22, v22
	v_exp_f32_e32 v23, v23
	v_exp_f32_e32 v24, v24
	v_exp_f32_e32 v25, v25
	v_exp_f32_e32 v26, v26
	v_exp_f32_e32 v27, v27
	v_mul_f32_e32 v100, v10, v20
	v_mul_f32_e32 v101, v10, v21
	v_mul_f32_e32 v102, v10, v22
	v_mul_f32_e32 v103, v10, v23
	v_mul_f32_e32 v116, v11, v24
	v_mul_f32_e32 v117, v11, v25
	v_mul_f32_e32 v118, v11, v26
	v_mul_f32_e32 v119, v11, v27
	v_add_u32_e32 v6, 0x8000, v6
	global_load_dwordx4 v[224:227], v6, s[12:13] offset:0 nt
	global_load_dwordx4 v[228:231], v6, s[12:13] offset:1024 nt
	global_load_dwordx4 v[232:235], v6, s[12:13] offset:2048 nt
	global_load_dwordx4 v[236:239], v6, s[12:13] offset:3072 nt
	v_mul_f32_e32 v16, v3, v3
	v_add_f32_e32 v17, 0x3f800000, v3
	v_add_f32_e32 v18, 0x40000000, v3
	v_add_f32_e32 v19, 0x40400000, v3
	v_mul_f32_e32 v17, v17, v17
	v_mul_f32_e32 v18, v18, v18
	v_mul_f32_e32 v19, v19, v19
	v_mul_f32_e32 v20, v28, v16
	v_mul_f32_e32 v24, v29, v16
	v_mul_f32_e32 v21, v28, v17
	v_mul_f32_e32 v25, v29, v17
	v_mul_f32_e32 v22, v28, v18
	v_mul_f32_e32 v26, v29, v18
	v_mul_f32_e32 v23, v28, v19
	v_mul_f32_e32 v27, v29, v19
	v_exp_f32_e32 v20, v20
	v_exp_f32_e32 v21, v21
	v_exp_f32_e32 v22, v22
	v_exp_f32_e32 v23, v23
	v_exp_f32_e32 v24, v24
	v_exp_f32_e32 v25, v25
	v_exp_f32_e32 v26, v26
	v_exp_f32_e32 v27, v27
	v_mul_f32_e32 v104, v30, v20
	v_mul_f32_e32 v105, v30, v21
	v_mul_f32_e32 v106, v30, v22
	v_mul_f32_e32 v107, v30, v23
	v_mul_f32_e32 v120, v31, v24
	v_mul_f32_e32 v121, v31, v25
	v_mul_f32_e32 v122, v31, v26
	v_mul_f32_e32 v123, v31, v27
	v_add_f32_e32 v16, 0x41800000, v3
	v_add_f32_e32 v17, 0x41880000, v3
	v_add_f32_e32 v18, 0x41900000, v3
	v_add_f32_e32 v19, 0x41980000, v3
	v_mul_f32_e32 v16, v16, v16
	v_mul_f32_e32 v17, v17, v17
	v_mul_f32_e32 v18, v18, v18
	v_mul_f32_e32 v19, v19, v19
	v_mul_f32_e32 v20, v28, v16
	v_mul_f32_e32 v24, v29, v16
	v_mul_f32_e32 v21, v28, v17
	v_mul_f32_e32 v25, v29, v17
	v_mul_f32_e32 v22, v28, v18
	v_mul_f32_e32 v26, v29, v18
	v_mul_f32_e32 v23, v28, v19
	v_mul_f32_e32 v27, v29, v19
	v_exp_f32_e32 v20, v20
	v_exp_f32_e32 v21, v21
	v_exp_f32_e32 v22, v22
	v_exp_f32_e32 v23, v23
	v_exp_f32_e32 v24, v24
	v_exp_f32_e32 v25, v25
	v_exp_f32_e32 v26, v26
	v_exp_f32_e32 v27, v27
	v_mul_f32_e32 v108, v30, v20
	v_mul_f32_e32 v109, v30, v21
	v_mul_f32_e32 v110, v30, v22
	v_mul_f32_e32 v111, v30, v23
	v_mul_f32_e32 v124, v31, v24
	v_mul_f32_e32 v125, v31, v25
	v_mul_f32_e32 v126, v31, v26
	v_mul_f32_e32 v127, v31, v27
	v_add_u32_e32 v6, 0x8000, v6
	global_load_dwordx4 v[240:243], v6, s[12:13] offset:0 nt
	global_load_dwordx4 v[244:247], v6, s[12:13] offset:1024 nt
	global_load_dwordx4 v[248:251], v6, s[12:13] offset:2048 nt
	global_load_dwordx4 v[252:255], v6, s[12:13] offset:3072 nt
	s_waitcnt vmcnt(28)
	v_add_f32_e32 v128, v128, v129
	v_add_f32_e32 v130, v130, v131
	v_add_f32_e32 v132, v132, v133
	v_add_f32_e32 v134, v134, v135
	v_add_f32_e32 v136, v136, v137
	v_add_f32_e32 v138, v138, v139
	v_add_f32_e32 v140, v140, v141
	v_add_f32_e32 v142, v142, v143
	v_add_f32_e32 v128, v128, v130
	v_add_f32_e32 v132, v132, v134
	v_add_f32_e32 v136, v136, v138
	v_add_f32_e32 v140, v140, v142
	v_cndmask_b32_e64 v130, v128, v132, s[30:31]
	v_cndmask_b32_e64 v134, v136, v140, s[30:31]
	v_cndmask_b32_e64 v129, v132, v128, s[30:31]
	v_cndmask_b32_e64 v133, v140, v136, s[30:31]
	v_add_f32_dpp v129, v130, v129 quad_perm:[1,0,3,2] row_mask:0xf bank_mask:0xf bound_ctrl:1
	v_add_f32_dpp v133, v134, v133 quad_perm:[1,0,3,2] row_mask:0xf bank_mask:0xf bound_ctrl:1
	v_cndmask_b32_e64 v135, v129, v133, s[32:33]
	v_cndmask_b32_e64 v131, v133, v129, s[32:33]
	s_nop 1
	v_add_f32_dpp v131, v135, v131 quad_perm:[2,3,0,1] row_mask:0xf bank_mask:0xf bound_ctrl:1
	v_cvt_f16_f32_e32 v131, v131
	ds_write_b16 v14, v131 offset:0
	s_waitcnt vmcnt(24)
	v_add_f32_e32 v144, v144, v145
	v_add_f32_e32 v146, v146, v147
	v_add_f32_e32 v148, v148, v149
	v_add_f32_e32 v150, v150, v151
	v_add_f32_e32 v152, v152, v153
	v_add_f32_e32 v154, v154, v155
	v_add_f32_e32 v156, v156, v157
	v_add_f32_e32 v158, v158, v159
	v_add_f32_e32 v144, v144, v146
	v_add_f32_e32 v148, v148, v150
	v_add_f32_e32 v152, v152, v154
	v_add_f32_e32 v156, v156, v158
	v_cndmask_b32_e64 v146, v144, v148, s[30:31]
	v_cndmask_b32_e64 v150, v152, v156, s[30:31]
	v_cndmask_b32_e64 v145, v148, v144, s[30:31]
	v_cndmask_b32_e64 v149, v156, v152, s[30:31]
	v_add_f32_dpp v145, v146, v145 quad_perm:[1,0,3,2] row_mask:0xf bank_mask:0xf bound_ctrl:1
	v_add_f32_dpp v149, v150, v149 quad_perm:[1,0,3,2] row_mask:0xf bank_mask:0xf bound_ctrl:1
	v_cndmask_b32_e64 v151, v145, v149, s[32:33]
	v_cndmask_b32_e64 v147, v149, v145, s[32:33]
	s_nop 1
	v_add_f32_dpp v147, v151, v147 quad_perm:[2,3,0,1] row_mask:0xf bank_mask:0xf bound_ctrl:1
	v_cvt_f16_f32_e32 v147, v147
	ds_write_b16 v14, v147 offset:1088
	s_waitcnt vmcnt(20)
	v_add_f32_e32 v160, v160, v161
	v_add_f32_e32 v162, v162, v163
	v_add_f32_e32 v164, v164, v165
	v_add_f32_e32 v166, v166, v167
	v_add_f32_e32 v168, v168, v169
	v_add_f32_e32 v170, v170, v171
	v_add_f32_e32 v172, v172, v173
	v_add_f32_e32 v174, v174, v175
	v_add_f32_e32 v160, v160, v162
	v_add_f32_e32 v164, v164, v166
	v_add_f32_e32 v168, v168, v170
	v_add_f32_e32 v172, v172, v174
	v_cndmask_b32_e64 v162, v160, v164, s[30:31]
	v_cndmask_b32_e64 v166, v168, v172, s[30:31]
	v_cndmask_b32_e64 v161, v164, v160, s[30:31]
	v_cndmask_b32_e64 v165, v172, v168, s[30:31]
	v_add_f32_dpp v161, v162, v161 quad_perm:[1,0,3,2] row_mask:0xf bank_mask:0xf bound_ctrl:1
	v_add_f32_dpp v165, v166, v165 quad_perm:[1,0,3,2] row_mask:0xf bank_mask:0xf bound_ctrl:1
	v_cndmask_b32_e64 v167, v161, v165, s[32:33]
	v_cndmask_b32_e64 v163, v165, v161, s[32:33]
	s_nop 1
	v_add_f32_dpp v163, v167, v163 quad_perm:[2,3,0,1] row_mask:0xf bank_mask:0xf bound_ctrl:1
	v_cvt_f16_f32_e32 v163, v163
	ds_write_b16 v14, v163 offset:2176
	s_waitcnt vmcnt(16)
	v_add_f32_e32 v176, v176, v177
	v_add_f32_e32 v178, v178, v179
	v_add_f32_e32 v180, v180, v181
	v_add_f32_e32 v182, v182, v183
	v_add_f32_e32 v184, v184, v185
	v_add_f32_e32 v186, v186, v187
	v_add_f32_e32 v188, v188, v189
	v_add_f32_e32 v190, v190, v191
	v_add_f32_e32 v176, v176, v178
	v_add_f32_e32 v180, v180, v182
	v_add_f32_e32 v184, v184, v186
	v_add_f32_e32 v188, v188, v190
	v_cndmask_b32_e64 v178, v176, v180, s[30:31]
	v_cndmask_b32_e64 v182, v184, v188, s[30:31]
	v_cndmask_b32_e64 v177, v180, v176, s[30:31]
	v_cndmask_b32_e64 v181, v188, v184, s[30:31]
	v_add_f32_dpp v177, v178, v177 quad_perm:[1,0,3,2] row_mask:0xf bank_mask:0xf bound_ctrl:1
	v_add_f32_dpp v181, v182, v181 quad_perm:[1,0,3,2] row_mask:0xf bank_mask:0xf bound_ctrl:1
	v_cndmask_b32_e64 v183, v177, v181, s[32:33]
	v_cndmask_b32_e64 v179, v181, v177, s[32:33]
	s_nop 1
	v_add_f32_dpp v179, v183, v179 quad_perm:[2,3,0,1] row_mask:0xf bank_mask:0xf bound_ctrl:1
	v_cvt_f16_f32_e32 v179, v179
	ds_write_b16 v14, v179 offset:3264
	s_mov_b32 s29, 0
	v_mov_b32_e32 v160, 0
	v_mov_b32_e32 v161, 0
	v_mov_b32_e32 v162, 0
	v_mov_b32_e32 v163, 0
	s_lshl_b32 s6, s6, 6
	s_add_i32 s6, s6, s7
	s_lshl_b32 s6, s6, 10
	v_add_u32_e32 v5, s6, v5
	s_branch .Lpass
